# v83: M3 retention epilogue rewritten in groups of four (no packed multiplies/pair moves/pads; row scale folded into the sigmoid reciprocal by one fma)
# speedup vs baseline: 1.0004x; 1.0004x over previous
.LBB0_556:
	v_cndmask_b32_e64 v34, 0, 1, s[4:5]
	s_lshl_b32 s4, s10, 6
	v_cmp_ne_u32_e32 vcc, 1, v34
	v_or_b32_e32 v34, s4, v108
	v_lshl_add_u32 v152, v34, 7, s58
	v_add_u32_e32 v38, v152, v120
	ds_read_b128 v[34:37], v38 offset:16384
	ds_read_b128 v[50:53], v38 offset:20480
	v_add_u32_e32 v148, v152, v121
	s_waitcnt vmcnt(3) lgkmcnt(1)
	v_mfma_f32_32x32x16_bf16 v[34:49], v[34:37], v[78:81], 0
	ds_read_b128 v[144:147], v148 offset:16384
	ds_read_b128 v[148:151], v148 offset:20480
	s_waitcnt lgkmcnt(2)
	v_mfma_f32_32x32x16_bf16 v[50:65], v[50:53], v[78:81], 0
	s_waitcnt vmcnt(2) lgkmcnt(1)
	v_mfma_f32_32x32x16_bf16 v[34:49], v[144:147], v[74:77], v[34:49]
	s_waitcnt lgkmcnt(0)
	v_mfma_f32_32x32x16_bf16 v[50:65], v[148:151], v[74:77], v[50:65]
	v_add_u32_e32 v148, v152, v122
	ds_read_b128 v[144:147], v148 offset:16384
	ds_read_b128 v[148:151], v148 offset:20480
	s_waitcnt vmcnt(1) lgkmcnt(1)
	v_mfma_f32_32x32x16_bf16 v[34:49], v[144:147], v[70:73], v[34:49]
	s_waitcnt lgkmcnt(0)
	v_mfma_f32_32x32x16_bf16 v[50:65], v[148:151], v[70:73], v[50:65]
	v_add_u32_e32 v148, v152, v123
	ds_read_b128 v[144:147], v148 offset:16384
	ds_read_b128 v[148:151], v148 offset:20480
	s_waitcnt vmcnt(0) lgkmcnt(1)
	v_mfma_f32_32x32x16_bf16 v[34:49], v[144:147], v[66:69], v[34:49]
	v_or_b32_e32 v145, s4, v82
	s_waitcnt lgkmcnt(0)
	v_mfma_f32_32x32x16_bf16 v[50:65], v[148:151], v[66:69], v[50:65]
	v_sub_u32_e32 v166, v109, v145
	v_cvt_f32_i32_e32 v166, v166
	v_mul_f32_e32 v175, v101, v166
	v_mul_f32_e64 v183, -v103, v166
	v_exp_f32_e32 v175, v175
	v_exp_f32_e32 v183, v183
	s_nop 0
	v_mul_f32_e32 v176, v175, v170
	v_mul_f32_e32 v184, v183, v174
	v_mul_f32_e32 v177, v176, v170
	v_mul_f32_e32 v185, v184, v174
	v_mul_f32_e32 v178, v177, v170
	v_mul_f32_e32 v186, v185, v174
	v_mul_f32_e32 v179, v178, v170
	v_mul_f32_e32 v187, v186, v174
	v_mul_f32_e32 v180, v179, v170
	v_mul_f32_e32 v188, v187, v174
	v_mul_f32_e32 v181, v180, v170
	v_mul_f32_e32 v189, v188, v174
	v_mul_f32_e32 v182, v181, v170
	v_mul_f32_e32 v190, v189, v174
	v_min_f32_e32 v160, v175, v183
	v_mul_f32_e32 v144, v34, v160
	v_min_f32_e32 v162, v179, v187
	v_mul_f32_e32 v34, v50, v162
	v_mul_f32_e32 v164, v175, v167
	v_mul_f32_e32 v165, v183, v171
	v_min_f32_e32 v164, v164, v165
	v_mul_f32_e32 v50, v35, v164
	v_mul_f32_e32 v160, v179, v167
	v_mul_f32_e32 v161, v187, v171
	v_min_f32_e32 v160, v160, v161
	v_mul_f32_e32 v35, v51, v160
	v_mul_f32_e32 v162, v175, v168
	v_mul_f32_e32 v163, v183, v172
	v_min_f32_e32 v162, v162, v163
	v_mul_f32_e32 v51, v36, v162
	v_mul_f32_e32 v164, v179, v168
	v_mul_f32_e32 v165, v187, v172
	v_min_f32_e32 v164, v164, v165
	v_mul_f32_e32 v36, v52, v164
	v_mul_f32_e32 v160, v175, v169
	v_mul_f32_e32 v161, v183, v173
	v_min_f32_e32 v160, v160, v161
	v_mul_f32_e32 v52, v37, v160
	v_mul_f32_e32 v162, v179, v169
	v_mul_f32_e32 v163, v187, v173
	v_min_f32_e32 v162, v162, v163
	v_mul_f32_e32 v37, v53, v162
	v_min_f32_e32 v164, v176, v184
	v_mul_f32_e32 v53, v38, v164
	v_min_f32_e32 v160, v180, v188
	v_mul_f32_e32 v38, v54, v160
	v_mul_f32_e32 v162, v176, v167
	v_mul_f32_e32 v163, v184, v171
	v_min_f32_e32 v162, v162, v163
	v_mul_f32_e32 v54, v39, v162
	v_mul_f32_e32 v164, v180, v167
	v_mul_f32_e32 v165, v188, v171
	v_min_f32_e32 v164, v164, v165
	v_mul_f32_e32 v39, v55, v164
	v_mul_f32_e32 v160, v176, v168
	v_mul_f32_e32 v161, v184, v172
	v_min_f32_e32 v160, v160, v161
	v_mul_f32_e32 v55, v40, v160
	v_mul_f32_e32 v162, v180, v168
	v_mul_f32_e32 v163, v188, v172
	v_min_f32_e32 v162, v162, v163
	v_mul_f32_e32 v40, v56, v162
	v_mul_f32_e32 v164, v176, v169
	v_mul_f32_e32 v165, v184, v173
	v_min_f32_e32 v164, v164, v165
	v_mul_f32_e32 v56, v41, v164
	v_mul_f32_e32 v160, v180, v169
	v_mul_f32_e32 v161, v188, v173
	v_min_f32_e32 v160, v160, v161
	v_mul_f32_e32 v41, v57, v160
	v_min_f32_e32 v162, v177, v185
	v_mul_f32_e32 v57, v42, v162
	v_min_f32_e32 v164, v181, v189
	v_mul_f32_e32 v42, v58, v164
	v_mul_f32_e32 v160, v177, v167
	v_mul_f32_e32 v161, v185, v171
	v_min_f32_e32 v160, v160, v161
	v_mul_f32_e32 v43, v43, v160
	v_mul_f32_e32 v162, v181, v167
	v_mul_f32_e32 v163, v189, v171
	v_min_f32_e32 v162, v162, v163
	v_mul_f32_e32 v58, v59, v162
	v_mul_f32_e32 v164, v177, v168
	v_mul_f32_e32 v165, v185, v172
	v_min_f32_e32 v164, v164, v165
	v_mul_f32_e32 v59, v44, v164
	v_mul_f32_e32 v160, v181, v168
	v_mul_f32_e32 v161, v189, v172
	v_min_f32_e32 v160, v160, v161
	v_mul_f32_e32 v60, v60, v160
	v_mul_f32_e32 v162, v177, v169
	v_mul_f32_e32 v163, v185, v173
	v_min_f32_e32 v162, v162, v163
	v_mul_f32_e32 v147, v45, v162
	v_mul_f32_e32 v164, v181, v169
	v_mul_f32_e32 v165, v189, v173
	v_min_f32_e32 v164, v164, v165
	v_mul_f32_e32 v61, v61, v164
	v_min_f32_e32 v160, v178, v186
	v_mul_f32_e32 v146, v46, v160
	v_min_f32_e32 v162, v182, v190
	v_mul_f32_e32 v62, v62, v162
	v_mul_f32_e32 v164, v178, v167
	v_mul_f32_e32 v165, v186, v171
	v_min_f32_e32 v164, v164, v165
	v_mul_f32_e32 v148, v47, v164
	v_mul_f32_e32 v160, v182, v167
	v_mul_f32_e32 v161, v190, v171
	v_min_f32_e32 v160, v160, v161
	v_mul_f32_e32 v63, v63, v160
	v_mul_f32_e32 v162, v178, v168
	v_mul_f32_e32 v163, v186, v172
	v_min_f32_e32 v162, v162, v163
	v_mul_f32_e32 v149, v48, v162
	v_mul_f32_e32 v164, v182, v168
	v_mul_f32_e32 v165, v190, v172
	v_min_f32_e32 v164, v164, v165
	v_mul_f32_e32 v64, v64, v164
	v_mul_f32_e32 v160, v178, v169
	v_mul_f32_e32 v161, v186, v173
	v_min_f32_e32 v160, v160, v161
	v_mul_f32_e32 v145, v49, v160
	v_mul_f32_e32 v162, v182, v169
	v_mul_f32_e32 v163, v190, v173
	v_min_f32_e32 v162, v162, v163
	v_mul_f32_e32 v65, v65, v162
	v_cvt_pk_bf16_f32 v44, v144, v50
	v_cvt_pk_bf16_f32 v45, v51, v52
	v_cvt_pk_bf16_f32 v46, v53, v54
	v_cvt_pk_bf16_f32 v47, v55, v56
	v_cvt_pk_bf16_f32 v48, v57, v43
	v_cvt_pk_bf16_f32 v49, v59, v147
	v_cvt_pk_bf16_f32 v50, v146, v148
	v_cvt_pk_bf16_f32 v51, v149, v145
	v_cvt_pk_bf16_f32 v34, v34, v35
	v_cvt_pk_bf16_f32 v35, v36, v37
	v_cvt_pk_bf16_f32 v36, v38, v39
	v_cvt_pk_bf16_f32 v37, v40, v41
	v_cvt_pk_bf16_f32 v38, v42, v58
	v_cvt_pk_bf16_f32 v39, v60, v61
	v_cvt_pk_bf16_f32 v40, v62, v63
	v_cvt_pk_bf16_f32 v41, v64, v65
	v_lshl_add_u32 v42, s10, 13, v110
	ds_read_b64_tr_b16 v[52:53], v42 offset:0
	ds_read_b64_tr_b16 v[54:55], v42 offset:0x400
	ds_read_b64_tr_b16 v[56:57], v42 offset:0x800
	ds_read_b64_tr_b16 v[58:59], v42 offset:0xc00
	ds_read_b64_tr_b16 v[60:61], v42 offset:0x1000
	ds_read_b64_tr_b16 v[62:63], v42 offset:0x1400
	ds_read_b64_tr_b16 v[144:145], v42 offset:0x1800
	ds_read_b64_tr_b16 v[146:147], v42 offset:0x1c00
	s_waitcnt lgkmcnt(0)
	v_permlane32_swap_b32_e32 v44, v46
	v_permlane32_swap_b32_e32 v45, v47
	v_permlane32_swap_b32_e32 v48, v50
	v_permlane32_swap_b32_e32 v49, v51
	v_permlane32_swap_b32_e32 v34, v36
	v_permlane32_swap_b32_e32 v35, v37
	v_permlane32_swap_b32_e32 v38, v40
	v_permlane32_swap_b32_e32 v39, v41
	v_mfma_f32_32x32x16_bf16 v[18:33], v[52:55], v[44:47], v[18:33]
	ds_read_b64_tr_b16 v[52:53], v42 offset:0x200
	ds_read_b64_tr_b16 v[54:55], v42 offset:0x600
	v_mfma_f32_32x32x16_bf16 v[18:33], v[56:59], v[48:51], v[18:33]
	ds_read_b64_tr_b16 v[56:57], v42 offset:0xa00
	ds_read_b64_tr_b16 v[58:59], v42 offset:0xe00
	v_mfma_f32_32x32x16_bf16 v[18:33], v[60:63], v[34:37], v[18:33]
	ds_read_b64_tr_b16 v[60:61], v42 offset:0x1200
	ds_read_b64_tr_b16 v[62:63], v42 offset:0x1600
	v_mfma_f32_32x32x16_bf16 v[18:33], v[144:147], v[38:41], v[18:33]
	ds_read_b64_tr_b16 v[144:145], v42 offset:0x1a00
	ds_read_b64_tr_b16 v[146:147], v42 offset:0x1e00
	s_waitcnt lgkmcnt(0)
	v_mfma_f32_32x32x16_bf16 v[2:17], v[52:55], v[44:47], v[2:17]
	s_mov_b64 s[4:5], 0
	s_and_b64 vcc, exec, vcc
	s_mov_b32 s10, 1
	v_mfma_f32_32x32x16_bf16 v[2:17], v[56:59], v[48:51], v[2:17]
	v_mfma_f32_32x32x16_bf16 v[2:17], v[60:63], v[34:37], v[2:17]
	v_mfma_f32_32x32x16_bf16 v[2:17], v[144:147], v[38:41], v[2:17]
	s_cbranch_vccz .LBB0_556
	v_mul_f32_e32 v34, v101, v111
	v_exp_f32_e32 v50, v34
	v_mul_f32_e32 v34, v103, v112
	v_exp_f32_e32 v51, v34
	v_lshlrev_b32_e32 v35, 16, v78
	v_and_b32_e32 v36, 0xffff0000, v78
	v_mul_f32_e32 v34, v50, v35
	v_mul_f32_e32 v37, v50, v36
	v_mul_f32_e32 v36, v51, v36
	v_cvt_pk_bf16_f32 v34, v34, v37
	v_mul_f32_e32 v35, v51, v35
	v_cvt_pk_bf16_f32 v38, v35, v36
	v_lshlrev_b32_e32 v36, 16, v79
	v_and_b32_e32 v37, 0xffff0000, v79
	v_mul_f32_e32 v35, v50, v36
	v_mul_f32_e32 v39, v50, v37
	v_mul_f32_e32 v37, v51, v37
	v_cvt_pk_bf16_f32 v35, v35, v39
	v_mul_f32_e32 v36, v51, v36
	v_cvt_pk_bf16_f32 v39, v36, v37
	v_lshlrev_b32_e32 v37, 16, v80
	v_and_b32_e32 v40, 0xffff0000, v80
	v_mul_f32_e32 v36, v50, v37
	v_mul_f32_e32 v41, v50, v40
	v_cvt_pk_bf16_f32 v36, v36, v41
	v_mul_f32_e32 v37, v51, v37
	v_mul_f32_e32 v40, v51, v40
	v_lshlrev_b32_e32 v41, 16, v81
	v_and_b32_e32 v42, 0xffff0000, v81
	v_cvt_pk_bf16_f32 v40, v37, v40
	v_mul_f32_e32 v37, v50, v41
	v_mul_f32_e32 v43, v50, v42
	v_mul_f32_e32 v41, v51, v41
	v_mul_f32_e32 v42, v51, v42
	v_cvt_pk_bf16_f32 v37, v37, v43
	v_cvt_pk_bf16_f32 v41, v41, v42
	ds_read_b128 v[42:45], v134 offset:32768
	ds_read_b128 v[46:49], v134 offset:40960
	s_waitcnt lgkmcnt(1)
	v_mfma_f32_32x32x16_bf16 v[18:33], v[42:45], v[34:37], v[18:33]
	s_mov_b64 s[4:5], 0x1400
	s_waitcnt lgkmcnt(0)
	v_mfma_f32_32x32x16_bf16 v[18:33], v[46:49], v[38:41], v[18:33]
	ds_read_b128 v[42:45], v134 offset:36864
	ds_read_b128 v[46:49], v134 offset:45056
	s_waitcnt lgkmcnt(1)
	v_mfma_f32_32x32x16_bf16 v[2:17], v[42:45], v[34:37], v[2:17]
	v_lshlrev_b32_e32 v35, 16, v74
	v_and_b32_e32 v36, 0xffff0000, v74
	v_mul_f32_e32 v34, v50, v35
	v_mul_f32_e32 v37, v50, v36
	v_mul_f32_e32 v36, v51, v36
	v_cvt_pk_bf16_f32 v34, v34, v37
	v_mul_f32_e32 v35, v51, v35
	s_waitcnt lgkmcnt(0)
	v_mfma_f32_32x32x16_bf16 v[2:17], v[46:49], v[38:41], v[2:17]
	v_cvt_pk_bf16_f32 v38, v35, v36
	v_lshlrev_b32_e32 v36, 16, v75
	v_and_b32_e32 v37, 0xffff0000, v75
	v_mul_f32_e32 v35, v50, v36
	v_mul_f32_e32 v39, v50, v37
	v_mul_f32_e32 v37, v51, v37
	v_cvt_pk_bf16_f32 v35, v35, v39
	v_mul_f32_e32 v36, v51, v36
	v_cvt_pk_bf16_f32 v39, v36, v37
	v_lshlrev_b32_e32 v37, 16, v76
	v_and_b32_e32 v40, 0xffff0000, v76
	v_mul_f32_e32 v36, v50, v37
	v_mul_f32_e32 v41, v50, v40
	v_cvt_pk_bf16_f32 v36, v36, v41
	v_mul_f32_e32 v37, v51, v37
	v_mul_f32_e32 v40, v51, v40
	v_lshlrev_b32_e32 v41, 16, v77
	v_and_b32_e32 v42, 0xffff0000, v77
	v_cvt_pk_bf16_f32 v40, v37, v40
	v_mul_f32_e32 v37, v50, v41
	v_mul_f32_e32 v43, v50, v42
	v_mul_f32_e32 v41, v51, v41
	v_mul_f32_e32 v42, v51, v42
	v_cvt_pk_bf16_f32 v37, v37, v43
	v_cvt_pk_bf16_f32 v41, v41, v42
	ds_read_b128 v[42:45], v135 offset:32768
	ds_read_b128 v[46:49], v135 offset:40960
	s_waitcnt lgkmcnt(1)
	v_mfma_f32_32x32x16_bf16 v[18:33], v[42:45], v[34:37], v[18:33]
	s_waitcnt lgkmcnt(0)
	v_mfma_f32_32x32x16_bf16 v[18:33], v[46:49], v[38:41], v[18:33]
	ds_read_b128 v[42:45], v135 offset:36864
	ds_read_b128 v[46:49], v135 offset:45056
	s_waitcnt lgkmcnt(1)
	v_mfma_f32_32x32x16_bf16 v[2:17], v[42:45], v[34:37], v[2:17]
	v_lshlrev_b32_e32 v35, 16, v70
	v_and_b32_e32 v36, 0xffff0000, v70
	v_mul_f32_e32 v34, v50, v35
	v_mul_f32_e32 v37, v50, v36
	v_mul_f32_e32 v36, v51, v36
	v_cvt_pk_bf16_f32 v34, v34, v37
	v_mul_f32_e32 v35, v51, v35
	s_waitcnt lgkmcnt(0)
	v_mfma_f32_32x32x16_bf16 v[2:17], v[46:49], v[38:41], v[2:17]
	v_cvt_pk_bf16_f32 v38, v35, v36
	v_lshlrev_b32_e32 v36, 16, v71
	v_and_b32_e32 v37, 0xffff0000, v71
	v_mul_f32_e32 v35, v50, v36
	v_mul_f32_e32 v39, v50, v37
	v_mul_f32_e32 v37, v51, v37
	v_cvt_pk_bf16_f32 v35, v35, v39
	v_mul_f32_e32 v36, v51, v36
	v_cvt_pk_bf16_f32 v39, v36, v37
	v_lshlrev_b32_e32 v37, 16, v72
	v_and_b32_e32 v40, 0xffff0000, v72
	v_mul_f32_e32 v36, v50, v37
	v_mul_f32_e32 v41, v50, v40
	v_cvt_pk_bf16_f32 v36, v36, v41
	v_mul_f32_e32 v37, v51, v37
	v_mul_f32_e32 v40, v51, v40
	v_lshlrev_b32_e32 v41, 16, v73
	v_and_b32_e32 v42, 0xffff0000, v73
	v_cvt_pk_bf16_f32 v40, v37, v40
	v_mul_f32_e32 v37, v50, v41
	v_mul_f32_e32 v43, v50, v42
	v_mul_f32_e32 v41, v51, v41
	v_mul_f32_e32 v42, v51, v42
	v_cvt_pk_bf16_f32 v37, v37, v43
	v_cvt_pk_bf16_f32 v41, v41, v42
	ds_read_b128 v[42:45], v136 offset:32768
	ds_read_b128 v[46:49], v136 offset:40960
	s_waitcnt lgkmcnt(1)
	v_mfma_f32_32x32x16_bf16 v[18:33], v[42:45], v[34:37], v[18:33]
	s_waitcnt lgkmcnt(0)
	v_mfma_f32_32x32x16_bf16 v[18:33], v[46:49], v[38:41], v[18:33]
	ds_read_b128 v[42:45], v136 offset:36864
	ds_read_b128 v[46:49], v136 offset:45056
	s_waitcnt lgkmcnt(1)
	v_mfma_f32_32x32x16_bf16 v[2:17], v[42:45], v[34:37], v[2:17]
	v_lshlrev_b32_e32 v35, 16, v66
	v_and_b32_e32 v36, 0xffff0000, v66
	v_mul_f32_e32 v34, v50, v35
	v_mul_f32_e32 v37, v50, v36
	v_mul_f32_e32 v36, v51, v36
	v_cvt_pk_bf16_f32 v34, v34, v37
	v_mul_f32_e32 v35, v51, v35
	s_waitcnt lgkmcnt(0)
	v_mfma_f32_32x32x16_bf16 v[2:17], v[46:49], v[38:41], v[2:17]
	v_cvt_pk_bf16_f32 v38, v35, v36
	v_lshlrev_b32_e32 v36, 16, v67
	v_and_b32_e32 v37, 0xffff0000, v67
	v_mul_f32_e32 v35, v50, v36
	v_mul_f32_e32 v39, v50, v37
	v_mul_f32_e32 v37, v51, v37
	v_cvt_pk_bf16_f32 v35, v35, v39
	v_mul_f32_e32 v36, v51, v36
	v_cvt_pk_bf16_f32 v39, v36, v37
	v_lshlrev_b32_e32 v37, 16, v68
	v_and_b32_e32 v40, 0xffff0000, v68
	v_mul_f32_e32 v36, v50, v37
	v_mul_f32_e32 v41, v50, v40
	v_cvt_pk_bf16_f32 v36, v36, v41
	v_mul_f32_e32 v37, v51, v37
	v_mul_f32_e32 v40, v51, v40
	v_lshlrev_b32_e32 v41, 16, v69
	v_and_b32_e32 v42, 0xffff0000, v69
	v_cvt_pk_bf16_f32 v40, v37, v40
	v_mul_f32_e32 v37, v50, v41
	v_mul_f32_e32 v43, v50, v42
	v_mul_f32_e32 v41, v51, v41
	v_mul_f32_e32 v42, v51, v42
	v_cvt_pk_bf16_f32 v37, v37, v43
	v_cvt_pk_bf16_f32 v41, v41, v42
	ds_read_b128 v[42:45], v137 offset:32768
	ds_read_b128 v[46:49], v137 offset:40960
	s_waitcnt lgkmcnt(1)
	v_mfma_f32_32x32x16_bf16 v[18:33], v[42:45], v[34:37], v[18:33]
	s_waitcnt lgkmcnt(0)
	v_mfma_f32_32x32x16_bf16 v[18:33], v[46:49], v[38:41], v[18:33]
	ds_read_b128 v[42:45], v137 offset:36864
	ds_read_b128 v[46:49], v137 offset:45056
	s_waitcnt lgkmcnt(1)
	v_mfma_f32_32x32x16_bf16 v[2:17], v[42:45], v[34:37], v[2:17]
	v_lshl_add_u64 v[34:35], s[22:23], 1, v[106:107]
	v_lshlrev_b32_e32 v36, 1, v82
	v_mov_b32_e32 v37, v0
	v_lshl_add_u64 v[34:35], v[34:35], 0, v[36:37]
	v_lshl_add_u64 v[36:37], v[34:35], 0, s[4:5]
	v_add_co_u32_e32 v34, vcc, s78, v34
	s_lshl_b64 s[4:5], s[24:25], 2
	s_nop 0
	v_addc_co_u32_e32 v35, vcc, 0, v35, vcc
	global_load_dwordx2 v[80:81], v[34:35], off offset:1024
	global_load_dwordx2 v[76:77], v[36:37], off offset:16
	global_load_dwordx2 v[74:75], v[36:37], off offset:32
	global_load_dwordx2 v[72:73], v[36:37], off offset:48
	global_load_dwordx2 v[70:71], v[36:37], off offset:64
	global_load_dwordx2 v[68:69], v[36:37], off offset:80
	global_load_dwordx2 v[66:67], v[36:37], off offset:96
	global_load_dwordx2 v[64:65], v[36:37], off offset:112
	ds_read_b32 v34, v0 offset:640
	ds_read_b32 v35, v0 offset:644
	s_waitcnt lgkmcnt(2)
	v_mfma_f32_32x32x16_bf16 v[2:17], v[46:49], v[38:41], v[2:17]
	v_mul_f32_e32 v78, v19, v19
	v_fmac_f32_e32 v78, v18, v18
	s_waitcnt lgkmcnt(1)
	v_readfirstlane_b32 s11, v34
	s_waitcnt lgkmcnt(0)
	v_readfirstlane_b32 s10, v35
	s_add_u32 s11, s11, s4
	s_addc_u32 s10, s10, s5
	s_lshl_b64 s[4:5], s[22:23], 2
	s_add_u32 s4, s11, s4
	s_addc_u32 s5, s10, s5
	v_lshlrev_b32_e32 v34, 2, v82
	global_load_dwordx4 v[144:147], v34, s[4:5]
	global_load_dwordx4 v[58:61], v34, s[4:5] offset:32
	global_load_dwordx4 v[54:57], v34, s[4:5] offset:64
	global_load_dwordx4 v[50:53], v34, s[4:5] offset:96
	global_load_dwordx4 v[46:49], v34, s[4:5] offset:128
	global_load_dwordx4 v[42:45], v34, s[4:5] offset:160
	global_load_dwordx4 v[38:41], v34, s[4:5] offset:192
	s_nop 0
	global_load_dwordx4 v[34:37], v34, s[4:5] offset:224
	v_fmac_f32_e32 v78, v20, v20
	v_fmac_f32_e32 v78, v21, v21
	v_fmac_f32_e32 v78, v22, v22
	v_fmac_f32_e32 v78, v23, v23
	v_fmac_f32_e32 v78, v24, v24
	v_fmac_f32_e32 v78, v25, v25
	v_fmac_f32_e32 v78, v26, v26
	v_fmac_f32_e32 v78, v27, v27
	v_fmac_f32_e32 v78, v28, v28
	v_fmac_f32_e32 v78, v29, v29
	v_fmac_f32_e32 v78, v30, v30
	v_fmac_f32_e32 v78, v31, v31
	v_fmac_f32_e32 v78, v32, v32
	v_fmac_f32_e32 v78, v33, v33
	v_fmac_f32_e32 v78, v2, v2
	v_fmac_f32_e32 v78, v3, v3
	v_fmac_f32_e32 v78, v4, v4
	v_fmac_f32_e32 v78, v5, v5
	v_fmac_f32_e32 v78, v6, v6
	v_fmac_f32_e32 v78, v7, v7
	v_fmac_f32_e32 v78, v8, v8
	v_fmac_f32_e32 v78, v9, v9
	v_fmac_f32_e32 v78, v10, v10
	v_fmac_f32_e32 v78, v11, v11
	v_fmac_f32_e32 v78, v12, v12
	v_fmac_f32_e32 v78, v13, v13
	v_fmac_f32_e32 v78, v14, v14
	v_fmac_f32_e32 v78, v15, v15
	v_pk_mul_f32 v[62:63], v[16:17], v[16:17]
	s_and_b64 vcc, exec, s[20:21]
	v_add_f32_e32 v62, v78, v62
	v_add_f32_e32 v62, v62, v63
	v_mov_b32_e32 v63, v62
	s_nop 1
	v_permlane32_swap_b32_e32 v62, v63
	v_add_f32_e32 v62, v62, v63
	v_fmamk_f32 v62, v62, 0x3c800000, v210
	v_rsq_f32_e32 v78, v62
	v_lshlrev_b64 v[62:63], 10, v[104:105]
	v_lshl_add_u64 v[62:63], s[82:83], 0, v[62:63]
	v_lshl_add_u64 v[62:63], v[62:63], 0, s[22:23]
	v_mul_f32_e32 v78, 0x41800000, v78
	v_lshl_add_u64 v[62:63], v[62:63], 0, v[84:85]
	v_rcp_f32_e32 v152, v78
	s_waitcnt vmcnt(7)
	v_lshlrev_b32_e32 v153, 16, v80
	v_and_b32_e32 v154, 0xffff0000, v80
	v_lshlrev_b32_e32 v155, 16, v81
	v_and_b32_e32 v156, 0xffff0000, v81
	v_mul_f32_e32 v157, 0xbfb8aa3b, v153
	v_mul_f32_e32 v158, 0xbfb8aa3b, v154
	v_mul_f32_e32 v159, 0xbfb8aa3b, v155
	v_mul_f32_e32 v160, 0xbfb8aa3b, v156
	v_exp_f32_e32 v157, v157
	v_exp_f32_e32 v158, v158
	v_exp_f32_e32 v159, v159
	v_exp_f32_e32 v160, v160
	v_mul_f32_e32 v161, v18, v144
	v_mul_f32_e32 v162, v19, v145
	v_mul_f32_e32 v163, v20, v146
	v_mul_f32_e32 v164, v21, v147
	v_fma_f32 v157, v157, v152, v152
	v_fma_f32 v158, v158, v152, v152
	v_fma_f32 v159, v159, v152, v152
	v_fma_f32 v160, v160, v152, v152
	v_rcp_f32_e32 v157, v157
	v_rcp_f32_e32 v158, v158
	v_rcp_f32_e32 v159, v159
	v_rcp_f32_e32 v160, v160
	v_mul_f32_e32 v153, v153, v157
	v_mul_f32_e32 v154, v154, v158
	v_mul_f32_e32 v155, v155, v159
	v_mul_f32_e32 v156, v156, v160
	v_mul_f32_e32 v161, v161, v153
	v_mul_f32_e32 v162, v162, v154
	v_mul_f32_e32 v163, v163, v155
	v_mul_f32_e32 v164, v164, v156
	v_cvt_pk_fp8_f32 v18, v161, v162
	v_cvt_pk_fp8_f32 v18, v163, v164 op_sel:[0,0,1]
	s_waitcnt vmcnt(6)
	v_lshlrev_b32_e32 v165, 16, v76
	v_and_b32_e32 v166, 0xffff0000, v76
	v_lshlrev_b32_e32 v167, 16, v77
	v_and_b32_e32 v168, 0xffff0000, v77
	v_mul_f32_e32 v169, 0xbfb8aa3b, v165
	v_mul_f32_e32 v170, 0xbfb8aa3b, v166
	v_mul_f32_e32 v171, 0xbfb8aa3b, v167
	v_mul_f32_e32 v172, 0xbfb8aa3b, v168
	v_exp_f32_e32 v169, v169
	v_exp_f32_e32 v170, v170
	v_exp_f32_e32 v171, v171
	v_exp_f32_e32 v172, v172
	v_mul_f32_e32 v173, v22, v58
	v_mul_f32_e32 v174, v23, v59
	v_mul_f32_e32 v175, v24, v60
	v_mul_f32_e32 v176, v25, v61
	v_fma_f32 v169, v169, v152, v152
	v_fma_f32 v170, v170, v152, v152
	v_fma_f32 v171, v171, v152, v152
	v_fma_f32 v172, v172, v152, v152
	v_rcp_f32_e32 v169, v169
	v_rcp_f32_e32 v170, v170
	v_rcp_f32_e32 v171, v171
	v_rcp_f32_e32 v172, v172
	v_mul_f32_e32 v165, v165, v169
	v_mul_f32_e32 v166, v166, v170
	v_mul_f32_e32 v167, v167, v171
	v_mul_f32_e32 v168, v168, v172
	v_mul_f32_e32 v173, v173, v165
	v_mul_f32_e32 v174, v174, v166
	v_mul_f32_e32 v175, v175, v167
	v_mul_f32_e32 v176, v176, v168
	v_cvt_pk_fp8_f32 v20, v173, v174
	v_cvt_pk_fp8_f32 v20, v175, v176 op_sel:[0,0,1]
	s_waitcnt vmcnt(5)
	v_lshlrev_b32_e32 v153, 16, v74
	v_and_b32_e32 v154, 0xffff0000, v74
	v_lshlrev_b32_e32 v155, 16, v75
	v_and_b32_e32 v156, 0xffff0000, v75
	v_mul_f32_e32 v157, 0xbfb8aa3b, v153
	v_mul_f32_e32 v158, 0xbfb8aa3b, v154
	v_mul_f32_e32 v159, 0xbfb8aa3b, v155
	v_mul_f32_e32 v160, 0xbfb8aa3b, v156
	v_exp_f32_e32 v157, v157
	v_exp_f32_e32 v158, v158
	v_exp_f32_e32 v159, v159
	v_exp_f32_e32 v160, v160
	v_mul_f32_e32 v161, v26, v54
	v_mul_f32_e32 v162, v27, v55
	v_mul_f32_e32 v163, v28, v56
	v_mul_f32_e32 v164, v29, v57
	v_fma_f32 v157, v157, v152, v152
	v_fma_f32 v158, v158, v152, v152
	v_fma_f32 v159, v159, v152, v152
	v_fma_f32 v160, v160, v152, v152
	v_rcp_f32_e32 v157, v157
	v_rcp_f32_e32 v158, v158
	v_rcp_f32_e32 v159, v159
	v_rcp_f32_e32 v160, v160
	v_mul_f32_e32 v153, v153, v157
	v_mul_f32_e32 v154, v154, v158
	v_mul_f32_e32 v155, v155, v159
	v_mul_f32_e32 v156, v156, v160
	v_mul_f32_e32 v161, v161, v153
	v_mul_f32_e32 v162, v162, v154
	v_mul_f32_e32 v163, v163, v155
	v_mul_f32_e32 v164, v164, v156
	v_cvt_pk_fp8_f32 v19, v161, v162
	v_cvt_pk_fp8_f32 v19, v163, v164 op_sel:[0,0,1]
	s_waitcnt vmcnt(4)
	v_lshlrev_b32_e32 v165, 16, v72
	v_and_b32_e32 v166, 0xffff0000, v72
	v_lshlrev_b32_e32 v167, 16, v73
	v_and_b32_e32 v168, 0xffff0000, v73
	v_mul_f32_e32 v169, 0xbfb8aa3b, v165
	v_mul_f32_e32 v170, 0xbfb8aa3b, v166
	v_mul_f32_e32 v171, 0xbfb8aa3b, v167
	v_mul_f32_e32 v172, 0xbfb8aa3b, v168
	v_exp_f32_e32 v169, v169
	v_exp_f32_e32 v170, v170
	v_exp_f32_e32 v171, v171
	v_exp_f32_e32 v172, v172
	v_mul_f32_e32 v173, v30, v50
	v_mul_f32_e32 v174, v31, v51
	v_mul_f32_e32 v175, v32, v52
	v_mul_f32_e32 v176, v33, v53
	v_fma_f32 v169, v169, v152, v152
	v_fma_f32 v170, v170, v152, v152
	v_fma_f32 v171, v171, v152, v152
	v_fma_f32 v172, v172, v152, v152
	v_rcp_f32_e32 v169, v169
	v_rcp_f32_e32 v170, v170
	v_rcp_f32_e32 v171, v171
	v_rcp_f32_e32 v172, v172
	v_mul_f32_e32 v165, v165, v169
	v_mul_f32_e32 v166, v166, v170
	v_mul_f32_e32 v167, v167, v171
	v_mul_f32_e32 v168, v168, v172
	v_mul_f32_e32 v173, v173, v165
	v_mul_f32_e32 v174, v174, v166
	v_mul_f32_e32 v175, v175, v167
	v_mul_f32_e32 v176, v176, v168
	v_cvt_pk_fp8_f32 v21, v173, v174
	v_cvt_pk_fp8_f32 v21, v175, v176 op_sel:[0,0,1]
	v_permlane32_swap_b32_e32 v18, v19
	s_nop 0
	v_permlane32_swap_b32_e32 v20, v21
	global_store_dwordx4 v[62:63], v[18:21], off offset:768
	s_waitcnt vmcnt(4)
	v_lshlrev_b32_e32 v153, 16, v70
	v_and_b32_e32 v154, 0xffff0000, v70
	v_lshlrev_b32_e32 v155, 16, v71
	v_and_b32_e32 v156, 0xffff0000, v71
	v_mul_f32_e32 v157, 0xbfb8aa3b, v153
	v_mul_f32_e32 v158, 0xbfb8aa3b, v154
	v_mul_f32_e32 v159, 0xbfb8aa3b, v155
	v_mul_f32_e32 v160, 0xbfb8aa3b, v156
	v_exp_f32_e32 v157, v157
	v_exp_f32_e32 v158, v158
	v_exp_f32_e32 v159, v159
	v_exp_f32_e32 v160, v160
	v_mul_f32_e32 v161, v2, v46
	v_mul_f32_e32 v162, v3, v47
	v_mul_f32_e32 v163, v4, v48
	v_mul_f32_e32 v164, v5, v49
	v_fma_f32 v157, v157, v152, v152
	v_fma_f32 v158, v158, v152, v152
	v_fma_f32 v159, v159, v152, v152
	v_fma_f32 v160, v160, v152, v152
	v_rcp_f32_e32 v157, v157
	v_rcp_f32_e32 v158, v158
	v_rcp_f32_e32 v159, v159
	v_rcp_f32_e32 v160, v160
	v_mul_f32_e32 v153, v153, v157
	v_mul_f32_e32 v154, v154, v158
	v_mul_f32_e32 v155, v155, v159
	v_mul_f32_e32 v156, v156, v160
	v_mul_f32_e32 v161, v161, v153
	v_mul_f32_e32 v162, v162, v154
	v_mul_f32_e32 v163, v163, v155
	v_mul_f32_e32 v164, v164, v156
	v_cvt_pk_fp8_f32 v2, v161, v162
	v_cvt_pk_fp8_f32 v2, v163, v164 op_sel:[0,0,1]
	s_waitcnt vmcnt(3)
	v_lshlrev_b32_e32 v165, 16, v68
	v_and_b32_e32 v166, 0xffff0000, v68
	v_lshlrev_b32_e32 v167, 16, v69
	v_and_b32_e32 v168, 0xffff0000, v69
	v_mul_f32_e32 v169, 0xbfb8aa3b, v165
	v_mul_f32_e32 v170, 0xbfb8aa3b, v166
	v_mul_f32_e32 v171, 0xbfb8aa3b, v167
	v_mul_f32_e32 v172, 0xbfb8aa3b, v168
	v_exp_f32_e32 v169, v169
	v_exp_f32_e32 v170, v170
	v_exp_f32_e32 v171, v171
	v_exp_f32_e32 v172, v172
	v_mul_f32_e32 v173, v6, v42
	v_mul_f32_e32 v174, v7, v43
	v_mul_f32_e32 v175, v8, v44
	v_mul_f32_e32 v176, v9, v45
	v_fma_f32 v169, v169, v152, v152
	v_fma_f32 v170, v170, v152, v152
	v_fma_f32 v171, v171, v152, v152
	v_fma_f32 v172, v172, v152, v152
	v_rcp_f32_e32 v169, v169
	v_rcp_f32_e32 v170, v170
	v_rcp_f32_e32 v171, v171
	v_rcp_f32_e32 v172, v172
	v_mul_f32_e32 v165, v165, v169
	v_mul_f32_e32 v166, v166, v170
	v_mul_f32_e32 v167, v167, v171
	v_mul_f32_e32 v168, v168, v172
	v_mul_f32_e32 v173, v173, v165
	v_mul_f32_e32 v174, v174, v166
	v_mul_f32_e32 v175, v175, v167
	v_mul_f32_e32 v176, v176, v168
	v_cvt_pk_fp8_f32 v4, v173, v174
	v_cvt_pk_fp8_f32 v4, v175, v176 op_sel:[0,0,1]
	s_waitcnt vmcnt(2)
	v_lshlrev_b32_e32 v153, 16, v66
	v_and_b32_e32 v154, 0xffff0000, v66
	v_lshlrev_b32_e32 v155, 16, v67
	v_and_b32_e32 v156, 0xffff0000, v67
	v_mul_f32_e32 v157, 0xbfb8aa3b, v153
	v_mul_f32_e32 v158, 0xbfb8aa3b, v154
	v_mul_f32_e32 v159, 0xbfb8aa3b, v155
	v_mul_f32_e32 v160, 0xbfb8aa3b, v156
	v_exp_f32_e32 v157, v157
	v_exp_f32_e32 v158, v158
	v_exp_f32_e32 v159, v159
	v_exp_f32_e32 v160, v160
	v_mul_f32_e32 v161, v10, v38
	v_mul_f32_e32 v162, v11, v39
	v_mul_f32_e32 v163, v12, v40
	v_mul_f32_e32 v164, v13, v41
	v_fma_f32 v157, v157, v152, v152
	v_fma_f32 v158, v158, v152, v152
	v_fma_f32 v159, v159, v152, v152
	v_fma_f32 v160, v160, v152, v152
	v_rcp_f32_e32 v157, v157
	v_rcp_f32_e32 v158, v158
	v_rcp_f32_e32 v159, v159
	v_rcp_f32_e32 v160, v160
	v_mul_f32_e32 v153, v153, v157
	v_mul_f32_e32 v154, v154, v158
	v_mul_f32_e32 v155, v155, v159
	v_mul_f32_e32 v156, v156, v160
	v_mul_f32_e32 v161, v161, v153
	v_mul_f32_e32 v162, v162, v154
	v_mul_f32_e32 v163, v163, v155
	v_mul_f32_e32 v164, v164, v156
	v_cvt_pk_fp8_f32 v3, v161, v162
	v_cvt_pk_fp8_f32 v3, v163, v164 op_sel:[0,0,1]
	s_waitcnt vmcnt(1)
	v_lshlrev_b32_e32 v165, 16, v64
	v_and_b32_e32 v166, 0xffff0000, v64
	v_lshlrev_b32_e32 v167, 16, v65
	v_and_b32_e32 v168, 0xffff0000, v65
	v_mul_f32_e32 v169, 0xbfb8aa3b, v165
	v_mul_f32_e32 v170, 0xbfb8aa3b, v166
	v_mul_f32_e32 v171, 0xbfb8aa3b, v167
	v_mul_f32_e32 v172, 0xbfb8aa3b, v168
	v_exp_f32_e32 v169, v169
	v_exp_f32_e32 v170, v170
	v_exp_f32_e32 v171, v171
	v_exp_f32_e32 v172, v172
	v_mul_f32_e32 v173, v14, v34
	v_mul_f32_e32 v174, v15, v35
	v_mul_f32_e32 v175, v16, v36
	v_mul_f32_e32 v176, v17, v37
	v_fma_f32 v169, v169, v152, v152
	v_fma_f32 v170, v170, v152, v152
	v_fma_f32 v171, v171, v152, v152
	v_fma_f32 v172, v172, v152, v152
	v_rcp_f32_e32 v169, v169
	v_rcp_f32_e32 v170, v170
	v_rcp_f32_e32 v171, v171
	v_rcp_f32_e32 v172, v172
	v_mul_f32_e32 v165, v165, v169
	v_mul_f32_e32 v166, v166, v170
	v_mul_f32_e32 v167, v167, v171
	v_mul_f32_e32 v168, v168, v172
	v_mul_f32_e32 v173, v173, v165
	v_mul_f32_e32 v174, v174, v166
	v_mul_f32_e32 v175, v175, v167
	v_mul_f32_e32 v176, v176, v168
	v_cvt_pk_fp8_f32 v5, v173, v174
	v_cvt_pk_fp8_f32 v5, v175, v176 op_sel:[0,0,1]
	v_permlane32_swap_b32_e32 v2, v3
	s_nop 0
	v_permlane32_swap_b32_e32 v4, v5
	global_store_dwordx4 v[62:63], v[2:5], off offset:800
	s_cbranch_vccz .LBB0_550
	s_waitcnt vmcnt(0)
	s_barrier
	s_and_saveexec_b64 s[4:5], s[0:1]
	s_cbranch_execz .LBB0_549
	s_mov_b64 s[10:11], exec
	v_mbcnt_lo_u32_b32 v2, s10, 0
	buffer_wbl2 sc1
	s_waitcnt vmcnt(0)
	s_waitcnt vmcnt(0)
	v_mbcnt_hi_u32_b32 v2, s11, v2
	v_cmp_eq_u32_e32 vcc, 0, v2
	s_and_b64 s[14:15], exec, vcc
	s_mov_b64 exec, s[14:15]
	s_cbranch_execz .LBB0_549
	s_bcnt1_i32_b64 s10, s[10:11]
	v_mov_b32_e32 v2, s10
	global_atomic_add v0, v2, s[84:85]
	s_branch .LBB0_549
